# baseline (speedup 1.0000x reference)
.LBB2_9:
	v_mad_i64_i32 v[0:1], s[12:13], v110, 48, 0
	v_or_b32_e32 v0, v0, v108
	v_lshlrev_b64 v[0:1], 8, v[0:1]
	v_lshl_add_u64 v[0:1], v[114:115], 0, v[0:1]
	v_add_co_u32_e32 v2, vcc, s15, v0
	global_load_dwordx4 v[24:27], v[0:1], off
	s_nop 0
	v_addc_co_u32_e32 v3, vcc, 0, v1, vcc
	v_add_co_u32_e32 v126, vcc, 0x2000, v0
	v_ashrrev_i32_e32 v111, 31, v110
	s_nop 0
	v_addc_co_u32_e32 v127, vcc, 0, v1, vcc
	global_load_dwordx4 v[64:67], v[2:3], off
	global_load_dwordx4 v[68:71], v[126:127], off
	global_load_dwordx4 v[20:23], v[0:1], off offset:64
	global_load_dwordx4 v[56:59], v[2:3], off offset:64
	global_load_dwordx4 v[60:63], v[126:127], off offset:64
	global_load_dwordx4 v[40:43], v[2:3], off offset:128
	global_load_dwordx4 v[16:19], v[0:1], off offset:128
	global_load_dwordx4 v[44:47], v[126:127], off offset:128
	global_load_dwordx4 v[28:31], v[2:3], off offset:192
	global_load_dwordx4 v[12:15], v[0:1], off offset:192
	global_load_dwordx4 v[32:35], v[126:127], off offset:192
	s_mov_b32 s12, 11
	v_mov_b32_e32 v72, v116
	s_mov_b32 s13, 0
	v_mov_b32_e32 v73, v109
	v_add_u32_e32 v121, v109, v112
	v_add_u32_e32 v122, 0x1f200, v112
	v_add_u32_e32 v124, v116, v112
	v_add_u32_e32 v124, 0x17600, v124
	v_mov_b32_e32 v0, 0
	v_mov_b32_e32 v1, v113
	v_mov_b32_e32 v2, v113
	v_mov_b32_e32 v3, v113
	v_mov_b32_e32 v36, 0
	v_mov_b32_e32 v37, v113
	v_mov_b32_e32 v38, v113
	v_mov_b32_e32 v39, v113
	v_mov_b32_e32 v48, 0
	v_mov_b32_e32 v49, v113
	v_mov_b32_e32 v50, v113
	v_mov_b32_e32 v51, v113
	v_mov_b32_e32 v52, 0
	v_mov_b32_e32 v53, v113
	v_mov_b32_e32 v54, v113
	v_mov_b32_e32 v55, v113
	v_mov_b32_e32 v4, 0
	v_mov_b32_e32 v5, v113
	v_mov_b32_e32 v6, v113
	v_mov_b32_e32 v7, v113
	v_mov_b32_e32 v8, 0
	v_mov_b32_e32 v9, v113
	v_mov_b32_e32 v10, v113
	v_mov_b32_e32 v11, v113
